# v18 + LDS bank-conflict-free swizzle for the dense diff K image: chunk position c ^ (r&7) ^ ((r>>4)&1)
# speedup vs baseline: 1.0073x; 1.0073x over previous
; #define LAS __attribute__((address_space(3)))
; __device__ __forceinline__ int v_rd_base(int lane) { return ((lane & 3) << 3) | (((lane >> 2) & 3) << 6) | (((lane >> 4) & 1) << 5) | (((lane >> 5) & 1) << 8); }
; #define DMA_WAIT(last) do { if (last) asm volatile("s_waitcnt vmcnt(0)" ::: "memory"); else asm volatile("s_waitcnt vmcnt(%0)" :: "n"(NPW) : "memory"); } while (0)
; template <int DK, int DV, bool OFF, class QLoader> ...
;     ...
;   QL.load(qr, wid * QBLK + r32, hi);
;   asm volatile("s_waitcnt vmcnt(0)" ::: "memory");
;   unsigned koff[KPW], voff[VPW];
; #pragma unroll
;   for (int i = 0; i < (DK == 64 ? 1 : KPW); ++i) { const int row = (wid * KPW + i) * 4 + (lane >> 4); int c = (lane & 15) ^ (row & 7); c = (c < DK / 8) ? c : (c & 7); koff[i] = (unsigned)((row * ldk) * 2 + c * 16); }
; #pragma unroll
;   for (int i = 0; i < 1; ++i) { const int sidx = (wid * VPW + i) * 2 + (lane >> 5), kg = sidx / ND, st = sidx % ND, kk = kg * 8 + ((lane & 31) >> 2);
;     const int k = (kk & ~0xC) | ((kk & 4) << 1) | ((kk & 8) >> 1), c = st * 32 + (lane & 3) * 8; voff[i] = (unsigned)((k * ldv + c) * 2); }
;   const int vb0 = (int)(uintptr_t)V_lds + v_rd_base(lane);
;   LAS unsigned* const ldsK = (LAS unsigned*)(LAS char*)K_lds + (wid * KPW) * 256; LAS unsigned* const ldsV = (LAS unsigned*)(LAS char*)V_lds + (wid * VPW) * 256;
;     ...
;   f32x16 pA0, pA1, pB0, pB1; bf16x8 pa0, pa1, pa2, pa3; const int NT = nkeys / KVBLK;
;   DMA_TILE(0, 0); DMA_TILE(1, 1); DMA_WAIT(false); __syncthreads(); if (2 < NT) DMA_TILE(2, 2);
;   qkt<DK>(pA0, pA1, K_lds, qr, r32, hi); partialSM<DK, OFF>(pA0, pA1, negMC);
; __device__ __forceinline__ void diff_attn_phase(Frame& F, const InPtrs& A, bool do_ctx, int conv_layer) {
;     ...
;         const bool lat = u < 2048; const int bh = lat ? (u >> 4) : (u - 2048), qb = lat ? (u & 15) : 0, b = bh >> 4, vh = bh & 15, h = vh >> 1;
;         const bf16* Qp = lat ? DQ + ((size_t)bh * 4096 + qb * 256) * 64 : DQC + (size_t)bh * 256 * 64;
;         const bf16* Kp = DKp + (size_t)bh * NKEYS * 64;
;         const bf16* V0 = QKV + (size_t)(NLAT + b * 256) * 3072 + 2048 + h * 128; const bf16* V1 = QKV + (size_t)(b * 4096) * 3072 + 2048 + h * 128;
;         bf16* Op = OB + (size_t)(lat ? b * 4096 + qb * 256 : NLAT + b * 256) * 2048 + vh * 128;
;         const att::QLoadPlain QL{Qp, 64};
.LBB0_838:
	s_and_b64 s[16:17], s[14:15], exec
	s_cselect_b32 s76, s12, s2
	s_ashr_i32 s2, s76, 4
	s_and_b32 s22, s76, 15
	s_mul_i32 s78, s76, 0x88000
	s_mul_hi_i32 s77, s76, 0x88000
	s_add_u32 s16, s65, s78
	s_addc_u32 s17, s66, s77
	s_lshl_b32 s4, s2, 8
	s_add_i32 s23, s4, 0x8000
	s_mul_i32 s80, s23, 0x1800
	s_mul_hi_i32 s79, s23, 0x1800
	s_add_u32 s4, s67, s80
	s_addc_u32 s12, s68, s79
	s_lshl_b32 s13, s76, 7
	s_and_b32 s13, s13, 0x700
	s_add_u32 s4, s4, s13
	s_addc_u32 s12, s12, 0
	s_add_u32 s18, s4, 0x1000
	s_addc_u32 s19, s12, 0
	s_lshl_b32 s12, s2, 12
	s_mul_i32 s2, s2, 0x1800000
	s_mul_hi_i32 s4, s12, 0x1800
	s_add_u32 s24, s67, s2
	s_addc_u32 s25, s68, s4
	s_add_u32 s13, s24, s13
	s_addc_u32 s24, s25, 0
	s_add_u32 s74, s13, 0x1000
	s_addc_u32 s75, s24, 0
	s_lshl_b32 s5, s5, 8
	s_or_b32 s5, s12, s5
	s_and_b64 s[12:13], s[14:15], exec
	s_cselect_b32 s12, s5, s23
	s_ashr_i32 s13, s12, 31
	s_lshl_b64 s[12:13], s[12:13], 12
	s_add_u32 s5, s69, s12
	s_addc_u32 s13, s70, s13
	s_lshl_b32 s12, s22, 8
	s_add_u32 s12, s5, s12
	s_addc_u32 s13, s13, 0
	s_andn2_b64 vcc, exec, s[34:35]
	s_mov_b64 s[22:23], -1
	s_cbranch_vccnz .LBB0_882
	v_mov_b32_e32 v25, v159
	v_mov_b32_e32 v33, v1
	v_readfirstlane_b32 s23, v25
	s_ashr_i32 s26, s23, 6
	v_and_b32_e32 v10, 31, v25
	s_lshl_b32 s22, s26, 5
	v_or_b32_e32 v2, s22, v10
	v_ashrrev_i32_e32 v3, 31, v2
	v_bfe_u32 v4, v25, 5, 1
	v_lshlrev_b64 v[2:3], 7, v[2:3]
	v_lshl_add_u64 v[2:3], s[20:21], 0, v[2:3]
	v_lshlrev_b32_e32 v32, 4, v4
	v_lshl_add_u64 v[2:3], v[2:3], 0, v[32:33]
	global_load_dwordx4 v[114:117], v[2:3], off
	global_load_dwordx4 v[118:121], v[2:3], off offset:32
	global_load_dwordx4 v[122:125], v[2:3], off offset:64
	global_load_dwordx4 v[126:129], v[2:3], off offset:96
	v_bfe_u32 v0, v25, 4, 2
	s_bfe_i32 s24, s26, 0x1001d
	v_and_b32_e32 v2, 15, v25
	v_bitop3_b32 v3, v0, v25, 15 bitop3:0x78
	v_lshl_or_b32 v20, s26, 2, v4
	s_lshr_b32 s24, s24, 30
	v_lshlrev_b32_e32 v3, 4, v3
	v_cmp_gt_u32_e32 vcc, 8, v2
	v_add_u32_e32 v2, s24, v20
	v_and_b32_e32 v5, 0x70, v3
	v_ashrrev_i32_e32 v21, 2, v2
	v_cndmask_b32_e32 v19, v5, v3, vcc
	v_lshlrev_b32_e32 v4, 3, v21
	v_bfe_u32 v5, v25, 2, 3
	v_bitop3_b32 v22, v4, -13, v5 bitop3:0xc8
	v_lshrrev_b32_e32 v4, 1, v25
	s_lshl_b32 s5, s26, 10
	v_lshlrev_b32_e32 v18, 7, v0
	v_and_b32_e32 v23, 8, v4
	v_and_b32_e32 v26, 4, v2
	v_or_b32_e32 v0, s5, v18
	v_and_b32_e32 v3, 0x3fffffc, v2
	v_or3_b32 v2, v23, v22, v26
	s_movk_i32 s24, 0xc00
	v_add_u32_e32 v0, v0, v19
	v_lshlrev_b32_e32 v4, 3, v25
	v_mul_lo_u32 v2, v2, s24
	s_add_i32 s27, 0, 0x10000
	s_lshl_b32 s24, s26, 11
	v_sub_u32_e32 v3, v20, v3
	v_and_b32_e32 v24, 24, v4
	s_add_i32 s81, s27, s5
	v_bfe_u32 v150, v25, 3, 3
	v_and_b32_e32 v0, 7, v25
	v_xor_b32_e32 v0, v0, v150
	v_bfe_u32 v151, v25, 7, 1
	v_xor_b32_e32 v0, v0, v151
	v_lshlrev_b32_e32 v0, 4, v0
	v_lshl_or_b32 v0, v150, 7, v0
	v_or_b32_e32 v0, s5, v0
	v_mov_b32_e32 v151, v1
	v_lshl_or_b32 v3, v3, 5, v24
	s_add_i32 s82, s24, 0
	s_mov_b32 m0, s81
	v_lshl_add_u64 v[4:5], s[16:17], 0, v[150:151]
	s_mov_b64 s[24:25], 0x200
	s_add_i32 s83, s81, 0x400
	v_add_lshl_u32 v148, v3, v2, 1
	global_load_lds_dwordx4 v0, s[16:17]
	v_lshl_add_u64 v[6:7], v[4:5], 0, s[24:25]
	s_mov_b32 m0, s83
	v_mov_b32_e32 v149, v1
	v_lshl_add_u64 v[6:7], s[18:19], 0, v[148:149]
	s_mov_b32 m0, s82
	s_add_i32 s84, s82, 0x400
	v_lshl_add_u64 v[2:3], s[16:17], 0, v[0:1]
	global_load_lds_dwordx4 v148, s[18:19]
	v_lshl_add_u64 v[8:9], v[6:7], 0, s[10:11]
	s_mov_b32 m0, s84
	s_mov_b64 s[24:25], 0x2000
	s_add_i32 s85, s81, 0x4000
	global_load_lds_dwordx4 v[8:9], off
	v_lshl_add_u64 v[8:9], v[2:3], 0, s[24:25]
	s_mov_b32 m0, s85
	s_mov_b64 s[24:25], 0x2200
	s_add_i32 s86, s81, 0x4400
	global_load_lds_dwordx4 v[8:9], off
	v_lshl_add_u64 v[8:9], v[4:5], 0, s[24:25]
	s_mov_b32 m0, s86
	s_mov_b64 s[24:25], 0x60000
	s_add_i32 s87, s82, 0x4000
	v_lshl_add_u64 v[8:9], v[6:7], 0, s[24:25]
	s_mov_b32 m0, s87
	s_mov_b64 s[24:25], 0x60080
	s_add_i32 s88, s82, 0x4400
	global_load_lds_dwordx4 v[8:9], off
	v_lshl_add_u64 v[8:9], v[6:7], 0, s[24:25]
	s_mov_b32 m0, s88
	s_mov_b64 s[24:25], 0x4000
	s_add_i32 s89, s81, 0x8000
	global_load_lds_dwordx4 v[8:9], off
	v_lshl_add_u64 v[2:3], v[2:3], 0, s[24:25]
	s_mov_b32 m0, s89
	s_mov_b64 s[24:25], 0x4200
	s_add_i32 s90, s81, 0x8400
	s_waitcnt vmcnt(4)
	s_waitcnt vmcnt(0) lgkmcnt(0)
	s_barrier
	global_load_lds_dwordx4 v[2:3], off
	v_lshl_add_u64 v[2:3], v[4:5], 0, s[24:25]
	s_mov_b32 m0, s90
	s_mov_b64 s[24:25], 0xc0000
	s_add_i32 s91, s82, 0x8000
	v_lshl_add_u64 v[2:3], v[6:7], 0, s[24:25]
	s_mov_b32 m0, s91
	s_mov_b64 s[24:25], 0xc0080
	s_add_i32 s92, s82, 0x8400
	global_load_lds_dwordx4 v[2:3], off
	v_lshl_add_u64 v[2:3], v[6:7], 0, s[24:25]
	s_mov_b32 m0, s92
	v_lshlrev_b32_e32 v27, 7, v10
	global_load_lds_dwordx4 v[2:3], off
	v_lshlrev_b32_e32 v2, 4, v25
	v_and_b32_e32 v33, 0x70, v2
	v_and_b32_e32 v2, 16, v25
	v_xor_b32_e32 v33, v33, v2
	v_bitop3_b32 v161, v32, v27, v33 bitop3:0xde
	v_add_u32_e32 v162, s27, v161
	ds_read_b128 v[2:5], v162
	ds_read_b128 v[28:31], v162 offset:4096
	s_waitcnt lgkmcnt(0)
	v_mfma_f32_32x32x16_bf16 v[66:81], v[28:31], v[114:117], 0
	v_or_b32_e32 v28, 32, v32
	v_bitop3_b32 v163, v28, v27, v33 bitop3:0xde
	v_add_u32_e32 v164, s27, v163
	ds_read_b128 v[28:31], v164
	s_cmp_lt_i32 s26, 4
	v_mfma_f32_32x32x16_bf16 v[2:17], v[2:5], v[114:117], 0
	s_waitcnt lgkmcnt(0)
	v_mfma_f32_32x32x16_bf16 v[2:17], v[28:31], v[118:121], v[2:17]
	ds_read_b128 v[28:31], v164 offset:4096
	s_waitcnt lgkmcnt(0)
	v_mfma_f32_32x32x16_bf16 v[66:81], v[28:31], v[118:121], v[66:81]
	v_or_b32_e32 v28, 64, v32
	v_bitop3_b32 v165, v28, v27, v33 bitop3:0xde
	v_add_u32_e32 v166, s27, v165
	ds_read_b128 v[28:31], v166
	s_waitcnt lgkmcnt(0)
	v_mfma_f32_32x32x16_bf16 v[2:17], v[28:31], v[122:125], v[2:17]
	ds_read_b128 v[28:31], v166 offset:4096
	s_waitcnt lgkmcnt(0)
	v_mfma_f32_32x32x16_bf16 v[66:81], v[28:31], v[122:125], v[66:81]
	v_or_b32_e32 v28, 0x60, v32
	v_bitop3_b32 v167, v28, v27, v33 bitop3:0xde
	v_add_u32_e32 v168, s27, v167
	ds_read_b128 v[28:31], v168
	s_waitcnt lgkmcnt(0)
	v_mfma_f32_32x32x16_bf16 v[2:17], v[28:31], v[126:129], v[2:17]
	ds_read_b128 v[28:31], v168 offset:4096
	s_waitcnt lgkmcnt(0)
	v_mfma_f32_32x32x16_bf16 v[66:81], v[28:31], v[126:129], v[66:81]
	s_cbranch_scc1 .LBB0_841
	s_setprio 1
